# kernel entry: the barrier-registration atomic's return is consumed at the first grid barrier instead of stalling wave 0 before the prologue's first loads
# speedup vs baseline: 1.0008x; 1.0008x over previous
.LBB0_2:
	s_add_i32 s2, 0, 0x20000
	v_lshl_add_u32 v2, v0, 2, s2
	v_mov_b32_e32 v1, 0
	v_or_b32_e32 v173, 0x400, v0
	ds_write2st64_b32 v2, v1, v1 offset1:8
	v_lshl_add_u32 v2, v173, 2, s2
	v_or_b32_e32 v171, 0x800, v0
	s_mov_b64 s[4:5], -1
	ds_write2st64_b32 v2, v1, v1 offset1:8
	s_and_saveexec_b64 s[6:7], s[4:5]
	v_lshl_add_u32 v2, v171, 2, 0
	v_add_u32_e32 v2, 0x20000, v2
	ds_write_b32 v2, v1
	s_or_b64 exec, exec, s[6:7]
	s_and_saveexec_b64 s[6:7], s[4:5]
	v_lshl_add_u32 v1, v171, 2, s2
	v_mov_b32_e32 v2, 0
	ds_write_b32 v1, v2 offset:2048
	s_or_b64 exec, exec, s[6:7]
	v_or_b32_e32 v1, 0xc00, v0
	v_cmp_gt_u32_e64 s[4:5], 7, 6
	v_cmp_gt_u32_e64 s[8:9], 7, 5
	s_and_saveexec_b64 s[6:7], s[8:9]
	v_lshl_add_u32 v2, v1, 2, 0
	v_add_u32_e32 v2, 0x20000, v2
	v_mov_b32_e32 v3, 0
	ds_write_b32 v2, v3
	s_or_b64 exec, exec, s[6:7]
	s_load_dwordx8 s[68:75], s[0:1], 0x80
	s_and_saveexec_b64 s[6:7], s[4:5]
	v_lshl_add_u32 v2, v1, 2, s2
	v_mov_b32_e32 v3, 0
	ds_write_b32 v2, v3 offset:2048
	s_or_b64 exec, exec, s[6:7]
	s_waitcnt lgkmcnt(0)
	s_add_u32 s2, s74, 0x4000
	s_load_dwordx2 s[94:95], s[0:1], 0xa0
	s_addc_u32 s3, s75, 0
	v_writelane_b32 v253, s2, 2
	s_waitcnt lgkmcnt(0)
	s_barrier
	v_writelane_b32 v253, s3, 3
	s_getreg_b32 s2, hwreg(HW_REG_XCC_ID, 0, 4)
	s_and_b32 s96, s2, 15
	v_cmp_ne_u32_e64 s[2:3], 0, v0
	s_nop 1
	v_writelane_b32 v253, s2, 4
	s_nop 1
	v_writelane_b32 v253, s3, 5
	v_cmp_eq_u32_e64 s[2:3], 0, v0
	s_mov_b64 s[4:5], exec
	s_nop 0
	v_writelane_b32 v253, s2, 6
	s_nop 1
	v_writelane_b32 v253, s3, 7
	s_and_b64 s[2:3], s[4:5], s[2:3]
	s_mov_b64 exec, s[2:3]
	s_cbranch_execz .LBB0_14
	s_mov_b64 s[8:9], exec
	v_mbcnt_lo_u32_b32 v2, s8, 0
	v_mbcnt_hi_u32_b32 v2, s9, v2
	v_cmp_eq_u32_e32 vcc, 0, v2
	s_and_saveexec_b64 s[6:7], vcc
	s_cbranch_execz .LBB0_13
	s_lshl_b32 s2, s96, 8
	s_bcnt1_i32_b64 s3, s[8:9]
	v_mov_b32_e32 v3, s2
	v_mov_b32_e32 v4, s3
	v_readlane_b32 s2, v253, 2
	v_readlane_b32 s3, v253, 3
	s_nop 4
	global_atomic_add v250, v3, v4, s[2:3] offset:1024 sc0
.LBB0_13:
	s_or_b64 exec, exec, s[6:7]
	v_mov_b32_e32 v251, v2

.LBB0_45:
	s_or_b64 exec, exec, s[0:1]
	s_waitcnt vmcnt(0)
	s_barrier
	s_mov_b64 s[0:1], exec
	v_readlane_b32 s2, v253, 6
	v_readlane_b32 s3, v253, 7
	s_and_b64 s[2:3], s[0:1], s[2:3]
	s_mov_b64 exec, s[2:3]
	s_cbranch_execz .LBB0_97
	v_readfirstlane_b32 s2, v250
	s_nop 1
	v_add_u32_e32 v251, s2, v251
	s_add_i32 s2, 0, 0x20168
	v_mov_b32_e32 v2, s2
	ds_write_b32 v2, v251
	s_add_i32 s2, 0, 0x20160
	v_mov_b32_e32 v2, s2
	s_waitcnt vmcnt(0) expcnt(0) lgkmcnt(0)
	ds_read_b32 v4, v2
	s_add_i32 s2, 0, 0x20164
	v_mov_b32_e32 v2, s2
	ds_read_b32 v2, v2
	s_waitcnt lgkmcnt(1)
	v_cmp_ne_u32_e32 vcc, 0, v4
	s_cbranch_vccnz .LBB0_61
	v_readlane_b32 s4, v253, 0
	v_readlane_b32 s5, v253, 1
	s_load_dwordx2 s[2:3], s[4:5], 0x4
	s_add_u32 s4, s74, 0x4200
	s_addc_u32 s5, s75, 0
	s_add_u32 s6, s74, 0x4400
	s_addc_u32 s7, s75, 0
	s_add_u32 s8, s74, 0x4500
	s_addc_u32 s9, s75, 0
	s_add_u32 s10, s74, 0x4600
	s_addc_u32 s11, s75, 0
	s_add_u32 s12, s74, 0x4700
	s_addc_u32 s13, s75, 0
	s_add_u32 s14, s74, 0x4800
	s_addc_u32 s15, s75, 0
	s_add_u32 s16, s74, 0x4900
	s_addc_u32 s17, s75, 0
	s_add_u32 s18, s74, 0x4a00
	s_addc_u32 s19, s75, 0
	s_add_u32 s20, s74, 0x4b00
	s_addc_u32 s21, s75, 0
	s_add_u32 s22, s74, 0x4c00
	s_addc_u32 s23, s75, 0
	s_add_u32 s36, s74, 0x4d00
	s_addc_u32 s37, s75, 0
	s_add_u32 s40, s74, 0x4e00
	s_addc_u32 s41, s75, 0
	s_add_u32 s54, s74, 0x4f00
	s_addc_u32 s55, s75, 0
	s_add_u32 s56, s74, 0x5000
	s_addc_u32 s57, s75, 0
	s_add_u32 s58, s74, 0x5100
	s_addc_u32 s59, s75, 0
	s_add_u32 s60, s74, 0x5200
	s_addc_u32 s61, s75, 0
	s_waitcnt lgkmcnt(0)
	s_mul_i32 s2, s2, s90
	s_add_u32 s62, s74, 0x5300
	s_mul_i32 s2, s2, s3
	s_addc_u32 s63, s75, 0
	s_mov_b32 s3, 1
	v_mov_b32_e32 v18, 0
	s_branch .LBB0_49
